# qk2
# speedup vs baseline: 1.0042x; 1.0042x over previous
.LBB3_39:
	v_cndmask_b32_e64 v231, v80, v180, s[6:7]
	v_mul_f32_e32 v180, 0xbe0293ee, v231
	v_fmamk_f32 v80, v100, 0x3e0293ee, v180
	v_fmamk_f32 v81, v101, 0x3e0293ee, v180
	v_fmamk_f32 v82, v102, 0x3e0293ee, v180
	v_fmamk_f32 v83, v103, 0x3e0293ee, v180
	v_fmamk_f32 v116, v104, 0x3e0293ee, v180
	v_fmamk_f32 v117, v105, 0x3e0293ee, v180
	v_fmamk_f32 v118, v106, 0x3e0293ee, v180
	v_fmamk_f32 v119, v107, 0x3e0293ee, v180
	v_fmamk_f32 v120, v108, 0x3e0293ee, v180
	v_fmamk_f32 v121, v109, 0x3e0293ee, v180
	v_fmamk_f32 v122, v110, 0x3e0293ee, v180
	v_fmamk_f32 v123, v111, 0x3e0293ee, v180
	v_fmamk_f32 v112, v112, 0x3e0293ee, v180
	v_fmamk_f32 v113, v113, 0x3e0293ee, v180
	v_fmamk_f32 v114, v114, 0x3e0293ee, v180
	v_fmamk_f32 v115, v115, 0x3e0293ee, v180
	v_fmamk_f32 v100, v84, 0x3e0293ee, v180
	v_fmamk_f32 v109, v85, 0x3e0293ee, v180
	v_fmamk_f32 v110, v86, 0x3e0293ee, v180
	v_fmamk_f32 v111, v87, 0x3e0293ee, v180
	v_fmamk_f32 v181, v88, 0x3e0293ee, v180
	v_fmamk_f32 v101, v89, 0x3e0293ee, v180
	v_fmamk_f32 v102, v90, 0x3e0293ee, v180
	v_fmamk_f32 v103, v91, 0x3e0293ee, v180
	v_fmamk_f32 v104, v92, 0x3e0293ee, v180
	v_fmamk_f32 v105, v93, 0x3e0293ee, v180
	v_fmamk_f32 v106, v94, 0x3e0293ee, v180
	v_fmamk_f32 v107, v95, 0x3e0293ee, v180
	v_exp_f32_e32 v80, v80
	v_exp_f32_e32 v81, v81
	v_exp_f32_e32 v82, v82
	v_exp_f32_e32 v83, v83
	v_exp_f32_e32 v84, v116
	v_exp_f32_e32 v85, v117
	v_exp_f32_e32 v86, v118
	v_exp_f32_e32 v87, v119
	v_exp_f32_e32 v88, v120
	v_exp_f32_e32 v89, v121
	v_exp_f32_e32 v90, v122
	v_exp_f32_e32 v91, v123
	v_exp_f32_e32 v92, v112
	v_exp_f32_e32 v93, v113
	v_exp_f32_e32 v94, v114
	v_exp_f32_e32 v95, v115
	v_fmamk_f32 v108, v96, 0x3e0293ee, v180
	v_fmamk_f32 v182, v97, 0x3e0293ee, v180
	v_fmamk_f32 v183, v98, 0x3e0293ee, v180
	v_fmac_f32_e32 v180, 0x3e0293ee, v99
	s_waitcnt lgkmcnt(0)
	s_barrier
	ds_read_b128 v[96:99], v217 offset:32768
	ds_read_b128 v[112:115], v217 offset:41472
	ds_read_b128 v[2:5], v217 offset:32800
	ds_read_b128 v[6:9], v217 offset:41504
	ds_read_b128 v[10:13], v217 offset:32832
	ds_read_b128 v[176:179], v217 offset:41536
	v_exp_f32_e32 v101, v101
	v_exp_f32_e32 v102, v102
	v_exp_f32_e32 v103, v103
	s_waitcnt lgkmcnt(5)
	v_mfma_f32_32x32x16_bf16 v[128:143], v[96:99], v[172:175], 0
	v_exp_f32_e32 v104, v104
	v_exp_f32_e32 v105, v105
	v_exp_f32_e32 v106, v106
	v_exp_f32_e32 v107, v107
	v_exp_f32_e32 v108, v108
	s_waitcnt lgkmcnt(4)
	v_mfma_f32_32x32x16_bf16 v[112:127], v[112:115], v[172:175], 0
	ds_read_b128 v[96:99], v217 offset:32864
	ds_read_b128 v[184:187], v217 offset:41568
	s_waitcnt lgkmcnt(5)
	v_mfma_f32_32x32x16_bf16 v[128:143], v[2:5], v[168:171], v[128:143]
	s_waitcnt lgkmcnt(4)
	v_mfma_f32_32x32x16_bf16 v[112:127], v[6:9], v[168:171], v[112:127]
	ds_read_b128 v[2:5], v217 offset:32896
	ds_read_b128 v[6:9], v217 offset:41600
	s_waitcnt lgkmcnt(5)
	v_mfma_f32_32x32x16_bf16 v[128:143], v[10:13], v[164:167], v[128:143]
	s_waitcnt lgkmcnt(4)
	v_mfma_f32_32x32x16_bf16 v[112:127], v[176:179], v[164:167], v[112:127]
	ds_read_b128 v[10:13], v217 offset:32928
	ds_read_b128 v[176:179], v217 offset:41632
	s_waitcnt lgkmcnt(5)
	v_mfma_f32_32x32x16_bf16 v[128:143], v[96:99], v[148:151], v[128:143]
	s_waitcnt lgkmcnt(4)
	v_mfma_f32_32x32x16_bf16 v[112:127], v[184:187], v[148:151], v[112:127]
	ds_read_b128 v[96:99], v217 offset:32960
	ds_read_b128 v[184:187], v217 offset:41664
	s_waitcnt lgkmcnt(5)
	v_mfma_f32_32x32x16_bf16 v[128:143], v[2:5], v[152:155], v[128:143]
	s_waitcnt lgkmcnt(4)
	v_mfma_f32_32x32x16_bf16 v[112:127], v[6:9], v[152:155], v[112:127]
	ds_read_b128 v[2:5], v217 offset:32992
	ds_read_b128 v[6:9], v217 offset:41696
	s_waitcnt lgkmcnt(5)
	v_mfma_f32_32x32x16_bf16 v[128:143], v[10:13], v[156:159], v[128:143]
	s_waitcnt lgkmcnt(4)
	v_mfma_f32_32x32x16_bf16 v[112:127], v[176:179], v[156:159], v[112:127]
	s_waitcnt lgkmcnt(3)
	v_mfma_f32_32x32x16_bf16 v[128:143], v[96:99], v[160:163], v[128:143]
	s_waitcnt lgkmcnt(2)
	v_mfma_f32_32x32x16_bf16 v[112:127], v[184:187], v[160:163], v[112:127]
	s_waitcnt lgkmcnt(1)
	v_mfma_f32_32x32x16_bf16 v[128:143], v[2:5], v[144:147], v[128:143]
	v_exp_f32_e32 v99, v111
	v_exp_f32_e32 v111, v180
	v_add_f32_e32 v180, 0, v80
	v_add_f32_e32 v180, v81, v180
	v_add_f32_e32 v180, v82, v180
	v_add_f32_e32 v180, v83, v180
	v_add_f32_e32 v180, v84, v180
	v_add_f32_e32 v180, v85, v180
	v_add_f32_e32 v180, v86, v180
	v_add_f32_e32 v180, v87, v180
	v_add_f32_e32 v180, v88, v180
	v_add_f32_e32 v180, v89, v180
	v_add_f32_e32 v180, v90, v180
	v_add_f32_e32 v180, v91, v180
	v_exp_f32_e32 v96, v100
	v_add_f32_e32 v180, v92, v180
	v_exp_f32_e32 v97, v109
	v_add_f32_e32 v180, v93, v180
	v_exp_f32_e32 v98, v110
	v_add_f32_e32 v180, v94, v180
	v_add_f32_e32 v180, v95, v180
	v_exp_f32_e32 v100, v181
	v_add_f32_e32 v180, v96, v180
	v_add_f32_e32 v180, v97, v180
	v_add_f32_e32 v180, v98, v180
	v_add_f32_e32 v180, v99, v180
	v_add_f32_e32 v180, v100, v180
	v_add_f32_e32 v180, v101, v180
	v_add_f32_e32 v180, v102, v180
	v_add_f32_e32 v180, v103, v180
	v_add_f32_e32 v180, v104, v180
	v_exp_f32_e32 v109, v182
	v_add_f32_e32 v180, v105, v180
	s_waitcnt lgkmcnt(0)
	v_mfma_f32_32x32x16_bf16 v[112:127], v[6:9], v[144:147], v[112:127]
	v_exp_f32_e32 v110, v183
	v_add_f32_e32 v180, v106, v180
	v_add_f32_e32 v180, v107, v180
	v_add_f32_e32 v180, v108, v180
	v_add_f32_e32 v180, v109, v180
	v_add_f32_e32 v180, v110, v180
	v_add_f32_e32 v232, v111, v180
	v_mov_b32_e32 v233, v232
	v_cvt_pk_bf16_f32 v180, v80, v81
	v_cvt_pk_bf16_f32 v181, v82, v83
	v_cvt_pk_bf16_f32 v182, v84, v85
	v_cvt_pk_bf16_f32 v183, v86, v87
	v_cvt_pk_bf16_f32 v184, v88, v89
	v_cvt_pk_bf16_f32 v185, v90, v91
	v_cvt_pk_bf16_f32 v186, v92, v93
	v_cvt_pk_bf16_f32 v187, v94, v95
	v_cvt_pk_bf16_f32 v188, v96, v97
	v_cvt_pk_bf16_f32 v189, v98, v99
	v_cvt_pk_bf16_f32 v190, v100, v101
	v_cvt_pk_bf16_f32 v191, v102, v103
	v_cvt_pk_bf16_f32 v192, v104, v105
	v_cvt_pk_bf16_f32 v193, v106, v107
	v_cvt_pk_bf16_f32 v194, v108, v109
	v_cvt_pk_bf16_f32 v195, v110, v111
	s_nop 1
	v_permlane32_swap_b32_e32 v232, v233
	v_permlane32_swap_b32_e32 v180, v182
	v_permlane32_swap_b32_e32 v181, v183
	v_permlane32_swap_b32_e32 v184, v186
	v_permlane32_swap_b32_e32 v185, v187
	v_permlane32_swap_b32_e32 v188, v190
	v_permlane32_swap_b32_e32 v189, v191
	v_permlane32_swap_b32_e32 v192, v194
	v_permlane32_swap_b32_e32 v193, v195
	s_add_i32 s6, s59, 1
	s_cmp_lt_i32 s6, s58
	s_cselect_b64 s[46:47], -1, 0
	s_cmp_ge_i32 s6, s58
	s_cbranch_scc1 .LBB3_41
	v_add_u32_e32 v2, 0x41, v234
	v_add_u32_e32 v4, 0x61, v234
	v_ashrrev_i32_e32 v3, 31, v2
	v_ashrrev_i32_e32 v5, 31, v4
	v_lshlrev_b64 v[10:11], 8, v[2:3]
	v_lshlrev_b64 v[12:13], 8, v[4:5]
	v_lshl_add_u64 v[2:3], v[14:15], 0, v[10:11]
	v_lshl_add_u64 v[6:7], v[14:15], 0, v[12:13]
	v_lshl_add_u64 v[10:11], v[208:209], 0, v[10:11]
	v_lshl_add_u64 v[176:177], v[208:209], 0, v[12:13]
	global_load_dwordx4 v[2:5], v[2:3], off
	s_nop 0
	global_load_dwordx4 v[6:9], v[6:7], off
	s_nop 0
	global_load_dwordx4 v[10:13], v[10:11], off
	s_nop 0
	global_load_dwordx4 v[176:179], v[176:177], off

.LBB3_51:
	s_and_b64 s[46:47], s[12:13], exec
	s_cselect_b32 s58, s28, s42
	s_cselect_b32 s59, s29, s43
	s_add_i32 s53, s53, 1
	s_cmp_lt_u32 s53, s11
	s_cselect_b64 s[46:47], -1, 0
	s_and_b64 s[46:47], s[46:47], exec
	s_cselect_b32 s57, s51, s57
	s_cselect_b32 s47, s43, s59
	s_cselect_b32 s46, s42, s58
	s_cselect_b32 s15, s41, s15
	s_cselect_b32 s14, s40, s14
	s_cselect_b32 s45, s39, s45
	s_cselect_b32 s44, s38, s44
	s_lshl_b32 s57, s57, 6
	v_or_b32_e32 v0, s57, v201
	v_lshlrev_b32_e32 v0, 8, v0
	v_lshl_add_u64 v[2:3], s[44:45], 0, v[0:1]
	v_mov_b32_e32 v199, v1
	v_add_lshl_u32 v4, s57, v210, 8
	v_mov_b32_e32 v5, v1
	v_lshl_add_u64 v[2:3], v[2:3], 0, v[198:199]
	v_lshl_add_u64 v[6:7], s[44:45], 0, v[4:5]
	v_lshl_add_u64 v[6:7], v[6:7], 0, v[198:199]
	global_load_dwordx4 v[120:123], v[2:3], off
	global_load_dwordx4 v[124:127], v[6:7], off
	v_lshl_add_u64 v[2:3], s[14:15], 0, v[0:1]
	v_lshl_add_u64 v[2:3], v[2:3], 0, v[198:199]
	v_lshl_add_u64 v[4:5], s[14:15], 0, v[4:5]
	v_lshl_add_u64 v[4:5], v[4:5], 0, v[198:199]
	global_load_dwordx4 v[112:115], v[2:3], off
	global_load_dwordx4 v[116:119], v[4:5], off
	v_or_b32_e32 v0, s8, v197
	v_lshlrev_b64 v[2:3], 8, v[0:1]
	v_lshl_add_u64 v[2:3], s[46:47], 0, v[2:3]
	v_mov_b32_e32 v207, v1
	v_lshl_add_u64 v[2:3], v[2:3], 0, v[206:207]
	global_load_dwordx4 v[172:175], v[2:3], off
	global_load_dwordx4 v[168:171], v[2:3], off offset:32
	global_load_dwordx4 v[164:167], v[2:3], off offset:64
	global_load_dwordx4 v[148:151], v[2:3], off offset:96
	global_load_dwordx4 v[152:155], v[2:3], off offset:128
	global_load_dwordx4 v[156:159], v[2:3], off offset:160
	global_load_dwordx4 v[160:163], v[2:3], off offset:192
	global_load_dwordx4 v[144:147], v[2:3], off offset:224
	v_add_f32_e32 v2, 0, v191
	v_add_f32_e32 v2, v193, v2
	v_add_f32_e32 v2, v189, v2
	v_add_f32_e32 v2, v192, v2
	v_add_f32_e32 v2, v188, v2
	v_add_f32_e32 v2, v190, v2
	v_add_f32_e32 v2, v186, v2
	v_add_f32_e32 v2, v187, v2
	v_add_f32_e32 v2, v179, v2
	v_add_f32_e32 v2, v184, v2
	v_add_f32_e32 v2, v177, v2
	v_add_f32_e32 v2, v182, v2
	v_exp_f32_e32 v10, v142
	v_add_f32_e32 v2, v176, v2
	v_exp_f32_e32 v11, v143
	v_add_f32_e32 v2, v185, v2
	v_exp_f32_e32 v12, v140
	v_add_f32_e32 v2, v178, v2
	v_exp_f32_e32 v13, v141
	v_add_f32_e32 v2, v183, v2
	v_exp_f32_e32 v14, v138
	v_add_f32_e32 v2, v10, v2
	v_exp_f32_e32 v15, v139
	v_add_f32_e32 v2, v11, v2
	v_exp_f32_e32 v136, v136
	v_add_f32_e32 v2, v12, v2
	v_exp_f32_e32 v137, v137
	v_add_f32_e32 v2, v13, v2
	v_exp_f32_e32 v134, v134
	v_add_f32_e32 v2, v14, v2
	v_exp_f32_e32 v135, v135
	v_add_f32_e32 v2, v15, v2
	v_exp_f32_e32 v132, v132
	v_add_f32_e32 v2, v136, v2
	v_exp_f32_e32 v133, v133
	v_add_f32_e32 v2, v137, v2
	v_exp_f32_e32 v130, v130
	v_add_f32_e32 v2, v134, v2
	v_exp_f32_e32 v131, v131
	v_add_f32_e32 v2, v135, v2
	v_exp_f32_e32 v138, v128
	v_add_f32_e32 v2, v132, v2
	v_exp_f32_e32 v139, v129
	v_add_f32_e32 v2, v133, v2
	v_add_f32_e32 v2, v130, v2
	v_add_f32_e32 v2, v131, v2
	v_add_f32_e32 v2, v138, v2
	v_add_f32_e32 v2, v139, v2
	v_mov_b32_e32 v3, v2
	s_nop 1
	v_permlane32_swap_b32_e32 v2, v3
	v_add_f32_e32 v181, v2, v3
	v_fmac_f32_e32 v181, v229, v228
	v_cvt_pk_bf16_f32 v2, v191, v193
	v_cvt_pk_bf16_f32 v3, v189, v192
	v_cvt_pk_bf16_f32 v4, v188, v190
	v_cvt_pk_bf16_f32 v5, v186, v187
	v_cvt_pk_bf16_f32 v6, v179, v184
	v_cvt_pk_bf16_f32 v7, v177, v182
	v_cvt_pk_bf16_f32 v8, v176, v185
	v_cvt_pk_bf16_f32 v9, v178, v183
	v_cvt_pk_bf16_f32 v10, v10, v11
	v_cvt_pk_bf16_f32 v11, v12, v13
	v_cvt_pk_bf16_f32 v12, v14, v15
	v_cvt_pk_bf16_f32 v13, v136, v137
	v_cvt_pk_bf16_f32 v128, v134, v135
	v_cvt_pk_bf16_f32 v129, v132, v133
	v_cvt_pk_bf16_f32 v130, v130, v131
	v_cvt_pk_bf16_f32 v131, v138, v139
	s_nop 0
	v_permlane32_swap_b32_e32 v2, v4
	v_permlane32_swap_b32_e32 v3, v5
	v_permlane32_swap_b32_e32 v6, v8
	v_permlane32_swap_b32_e32 v7, v9
	v_permlane32_swap_b32_e32 v10, v12
	v_permlane32_swap_b32_e32 v11, v13
	v_permlane32_swap_b32_e32 v128, v130
	v_permlane32_swap_b32_e32 v129, v131
	ds_read_b64_tr_b16 v[132:133], v213 offset:0
	ds_read_b64_tr_b16 v[134:135], v213 offset:0x800
	ds_read_b64_tr_b16 v[136:137], v213 offset:0x1000
	ds_read_b64_tr_b16 v[138:139], v213 offset:0x1800
	ds_read_b64_tr_b16 v[140:141], v213 offset:0x2000
	ds_read_b64_tr_b16 v[142:143], v213 offset:0x2800
	ds_read_b64_tr_b16 v[176:177], v213 offset:0x3000
	ds_read_b64_tr_b16 v[178:179], v213 offset:0x3800
	s_waitcnt lgkmcnt(0)
	s_nop 0
	v_mfma_f32_32x32x16_bf16 v[64:79], v[2:5], v[132:135], v[64:79]
	ds_read_b64_tr_b16 v[132:133], v213 offset:0x200
	ds_read_b64_tr_b16 v[134:135], v213 offset:0xa00
	v_mfma_f32_32x32x16_bf16 v[64:79], v[6:9], v[136:139], v[64:79]
	ds_read_b64_tr_b16 v[136:137], v213 offset:0x1200
	ds_read_b64_tr_b16 v[138:139], v213 offset:0x1a00
	v_mfma_f32_32x32x16_bf16 v[64:79], v[10:13], v[140:143], v[64:79]
	ds_read_b64_tr_b16 v[140:141], v213 offset:0x2200
	ds_read_b64_tr_b16 v[142:143], v213 offset:0x2a00
	ds_read_b64_tr_b16 v[182:183], v213 offset:0x3200
	ds_read_b64_tr_b16 v[184:185], v213 offset:0x3a00
	s_waitcnt lgkmcnt(0)
	v_mfma_f32_32x32x16_bf16 v[64:79], v[128:131], v[176:179], v[64:79]
	v_mfma_f32_32x32x16_bf16 v[48:63], v[2:5], v[132:135], v[48:63]
	ds_read_b64_tr_b16 v[132:133], v213 offset:0x400
	ds_read_b64_tr_b16 v[134:135], v213 offset:0xc00
	v_mfma_f32_32x32x16_bf16 v[48:63], v[6:9], v[136:139], v[48:63]
	ds_read_b64_tr_b16 v[136:137], v213 offset:0x1400
	ds_read_b64_tr_b16 v[138:139], v213 offset:0x1c00
	v_mfma_f32_32x32x16_bf16 v[48:63], v[10:13], v[140:143], v[48:63]
	ds_read_b64_tr_b16 v[140:141], v213 offset:0x2400
	ds_read_b64_tr_b16 v[142:143], v213 offset:0x2c00
	ds_read_b64_tr_b16 v[176:177], v213 offset:0x3400
	ds_read_b64_tr_b16 v[178:179], v213 offset:0x3c00
	s_waitcnt lgkmcnt(0)
	v_mfma_f32_32x32x16_bf16 v[48:63], v[128:131], v[182:185], v[48:63]
	v_mfma_f32_32x32x16_bf16 v[32:47], v[2:5], v[132:135], v[32:47]
	ds_read_b64_tr_b16 v[132:133], v213 offset:0x600
	ds_read_b64_tr_b16 v[134:135], v213 offset:0xe00
	v_mfma_f32_32x32x16_bf16 v[32:47], v[6:9], v[136:139], v[32:47]
	ds_read_b64_tr_b16 v[136:137], v213 offset:0x1600
	ds_read_b64_tr_b16 v[138:139], v213 offset:0x1e00
	v_mfma_f32_32x32x16_bf16 v[32:47], v[10:13], v[140:143], v[32:47]
	ds_read_b64_tr_b16 v[140:141], v213 offset:0x2600
	ds_read_b64_tr_b16 v[142:143], v213 offset:0x2e00
	ds_read_b64_tr_b16 v[182:183], v213 offset:0x3600
	ds_read_b64_tr_b16 v[184:185], v213 offset:0x3e00
	s_waitcnt lgkmcnt(0)
	v_mfma_f32_32x32x16_bf16 v[32:47], v[128:131], v[176:179], v[32:47]
	v_mfma_f32_32x32x16_bf16 v[16:31], v[2:5], v[132:135], v[16:31]
	s_andn2_b64 vcc, exec, s[6:7]
	v_mfma_f32_32x32x16_bf16 v[16:31], v[6:9], v[136:139], v[16:31]
	v_mfma_f32_32x32x16_bf16 v[16:31], v[10:13], v[140:143], v[16:31]
	v_mfma_f32_32x32x16_bf16 v[16:31], v[128:131], v[182:185], v[16:31]
	s_cbranch_vccnz .LBB3_59
	s_lshl_b32 s7, s54, 6
	s_sub_i32 s6, s7, 64
	s_add_i32 s7, s7, -1
	s_cmp_le_i32 s7, s55
	s_cselect_b64 s[14:15], -1, 0
	s_cmp_gt_i32 s6, s56
	s_cselect_b64 s[44:45], -1, 0
	s_and_b64 s[14:15], s[14:15], s[44:45]
	s_and_b64 vcc, exec, s[14:15]
	s_cbranch_vccnz .LBB3_54
	v_subrev_u32_e32 v2, s6, v227
	v_cmp_ge_i32_e64 s[64:65], v2, 0
	v_cmp_ge_i32_e64 s[66:67], v2, 32
	v_cmp_ge_i32_e64 s[68:69], v2, 1
	v_cmp_ge_i32_e64 s[70:71], v2, 33
	v_cmp_ge_i32_e64 s[72:73], v2, 2
	v_cmp_ge_i32_e64 s[74:75], v2, 34
	v_cmp_ge_i32_e64 s[76:77], v2, 3
	v_cmp_ge_i32_e64 s[78:79], v2, 35
	v_cndmask_b32_e64 v80, v221, v80, s[64:65]
	v_cndmask_b32_e64 v96, v221, v96, s[66:67]
	v_cndmask_b32_e64 v81, v221, v81, s[68:69]
	v_cndmask_b32_e64 v97, v221, v97, s[70:71]
	v_cndmask_b32_e64 v82, v221, v82, s[72:73]
	v_cndmask_b32_e64 v98, v221, v98, s[74:75]
	v_cndmask_b32_e64 v83, v221, v83, s[76:77]
	v_cndmask_b32_e64 v99, v221, v99, s[78:79]
	v_cmp_ge_i32_e64 s[64:65], v2, 8
	v_cmp_ge_i32_e64 s[66:67], v2, 40
	v_cmp_ge_i32_e64 s[68:69], v2, 9
	v_cmp_ge_i32_e64 s[70:71], v2, 41
	v_cmp_ge_i32_e64 s[72:73], v2, 10
	v_cmp_ge_i32_e64 s[74:75], v2, 42
	v_cmp_ge_i32_e64 s[76:77], v2, 11
	v_cmp_ge_i32_e64 s[78:79], v2, 43
	v_cndmask_b32_e64 v84, v221, v84, s[64:65]
	v_cndmask_b32_e64 v100, v221, v100, s[66:67]
	v_cndmask_b32_e64 v85, v221, v85, s[68:69]
	v_cndmask_b32_e64 v101, v221, v101, s[70:71]
	v_cndmask_b32_e64 v86, v221, v86, s[72:73]
	v_cndmask_b32_e64 v102, v221, v102, s[74:75]
	v_cndmask_b32_e64 v87, v221, v87, s[76:77]
	v_cndmask_b32_e64 v103, v221, v103, s[78:79]
	v_cmp_ge_i32_e64 s[64:65], v2, 16
	v_cmp_ge_i32_e64 s[66:67], v2, 48
	v_cmp_ge_i32_e64 s[68:69], v2, 17
	v_cmp_ge_i32_e64 s[70:71], v2, 49
	v_cmp_ge_i32_e64 s[72:73], v2, 18
	v_cmp_ge_i32_e64 s[74:75], v2, 50
	v_cmp_ge_i32_e64 s[76:77], v2, 19
	v_cmp_ge_i32_e64 s[78:79], v2, 51
	v_cndmask_b32_e64 v88, v221, v88, s[64:65]
	v_cndmask_b32_e64 v104, v221, v104, s[66:67]
	v_cndmask_b32_e64 v89, v221, v89, s[68:69]
	v_cndmask_b32_e64 v105, v221, v105, s[70:71]
	v_cndmask_b32_e64 v90, v221, v90, s[72:73]
	v_cndmask_b32_e64 v106, v221, v106, s[74:75]
	v_cndmask_b32_e64 v91, v221, v91, s[76:77]
	v_cndmask_b32_e64 v107, v221, v107, s[78:79]
	v_cmp_ge_i32_e64 s[64:65], v2, 24
	v_cmp_ge_i32_e64 s[66:67], v2, 56
	v_cmp_ge_i32_e64 s[68:69], v2, 25
	v_cmp_ge_i32_e64 s[70:71], v2, 57
	v_cmp_ge_i32_e64 s[72:73], v2, 26
	v_cmp_ge_i32_e64 s[74:75], v2, 58
	v_cmp_ge_i32_e64 s[76:77], v2, 27
	v_cmp_ge_i32_e64 s[78:79], v2, 59
	v_cndmask_b32_e64 v92, v221, v92, s[64:65]
	v_cndmask_b32_e64 v108, v221, v108, s[66:67]
	v_cndmask_b32_e64 v93, v221, v93, s[68:69]
	v_cndmask_b32_e64 v109, v221, v109, s[70:71]
	v_cndmask_b32_e64 v94, v221, v94, s[72:73]
	v_cndmask_b32_e64 v110, v221, v110, s[74:75]
	v_cndmask_b32_e64 v95, v221, v95, s[76:77]
	v_cndmask_b32_e64 v111, v221, v111, s[78:79]
